# attention tile loop hand-rewritten: VALU segment | barrier | MFMA segment, waves 4-7 one segment behind
# speedup vs baseline: 1.0202x; 1.0202x over previous
; #define LAS __attribute__((address_space(3)))
; __device__ __forceinline__ void lds_barrier() { asm volatile("s_waitcnt lgkmcnt(0)" ::: "memory"); __builtin_amdgcn_s_barrier(); asm volatile("" ::: "memory"); }
; #define AT_LOADK(t) do { const int kr_ = AT_KROW(t); _Pragma("unroll") for (int i_ = 0; i_ < 2; ++i_) kreg[i_] = *(const u32x4*)(Kp + (size_t)(kr_ + prow0 + 32 * i_) * 512 + pch * 8); } while (0)
; #define AT_LOADV(t) do { const int kr_ = AT_KROW(t); _Pragma("unroll") for (int i_ = 0; i_ < 2; ++i_) vreg[i_] = *(const u32x4*)(Vp + (size_t)(kr_ + prow0 + 32 * i_) * 512 + pch * 8); } while (0)
; #define AT_STOREK(st) do { _Pragma("unroll") for (int i_ = 0; i_ < 2; ++i_) *(LAS u32x4*)(L + AT_K + (st) * AT_KBYTES + (prow0 + 32 * i_) * AT_KSTR + pch * 16) = kreg[i_]; } while (0)
; #define AT_STOREV(st) do { _Pragma("unroll") for (int i_ = 0; i_ < 2; ++i_) *(LAS u32x4*)(L + AT_V + (st) * AT_VBYTES + (prow0 + 32 * i_) * AT_VSTR + pch * 16) = vreg[i_]; } while (0)
; __device__ __forceinline__ void attn_unit(const Frame& F, int layer, int qrow0, int ntiles, int b, int head, float lam, float m2, float lam_init) {
;     int tid_ = F.tid; asm volatile("" : "+v"(tid_));
;     const int tid = tid_, lane = tid & 63, wave = __builtin_amdgcn_readfirstlane(tid >> 6), r32 = lane & 31, hh = lane >> 5;
;     const int mp = wave & 1, qg = wave >> 1;
;     LAS unsigned char* L = F.lds;
;     const bf16_t* const Kp = F_K + head * 128; const bf16_t* const Vp = F_V + head * 128; bf16_t* const A2p = F_A2;
;     bf16x8 qf[4];
;     { const bf16_t* qp = F_Q + (size_t)(qrow0 + 32 * qg + r32) * 512 + head * 128 + mp * 64 + 8 * hh;
; #pragma unroll
;       for (int d0 = 0; d0 < 4; ++d0) qf[d0] = *(const bf16x8*)(qp + d0 * 16); }
;     f32x16 o[4];
; #pragma unroll
;     for (int j = 0; j < 4; ++j) o[j] = (f32x16){};
;     float lsum = 0.f;
;     f32x16 negm;
;     { float m2l = m2; asm volatile("" : "+v"(m2l));
; #pragma unroll
;       for (int t = 0; t < 16; ++t) negm[t] = -m2l; }
;     u32x4 kreg[2], vreg[2];
;     const int prow0 = tid >> 4, pch = tid & 15;
;     ...
;     if (wave >= 4) __builtin_amdgcn_s_setprio(1);
;     AT_LOADK(0); AT_LOADV(0); AT_STOREK(0); AT_STOREV(0);
;     if (ntiles > 1) { AT_LOADK(1); AT_STOREK(1); }
;     __syncthreads();
;     f32x16 sa, sb, na, nb;
;     AT_QK(sa, sb, 0);
;     lds_barrier();
.LBB0_549:
	s_add_u32 s42, s4, s30
	s_addc_u32 s43, s5, 0
	s_add_u32 s2, s2, s30
	s_addc_u32 s3, s3, 0
	s_lshl_b32 s4, s16, 8
	v_ashrrev_i32_e32 v186, 4, v32
	s_add_i32 s5, s4, 0x8000
	s_add_i32 s16, s4, 0x8040
	v_lshlrev_b32_e32 v3, 4, v32
	v_add_u32_e32 v128, s5, v186
	v_and_b32_e32 v144, 0xf0, v3
	v_add_u32_e32 v20, s16, v186
	v_lshl_add_u64 v[4:5], s[2:3], 0, v[144:145]
	s_mov_b64 s[2:3], 0x31534800
	v_ashrrev_i32_e32 v129, 31, v128
	v_ashrrev_i32_e32 v21, 31, v20
	v_lshl_add_u64 v[180:181], v[4:5], 0, s[2:3]
	v_lshlrev_b64 v[12:13], 10, v[128:129]
	s_mov_b64 s[2:3], 0x8000
	v_lshl_add_u64 v[16:17], s[42:43], 0, v[144:145]
	s_mov_b64 s[42:43], 0x33934800
	v_lshlrev_b64 v[62:63], 10, v[20:21]
	v_lshl_add_u64 v[14:15], v[12:13], 0, s[2:3]
	v_lshl_add_u64 v[182:183], v[16:17], 0, s[42:43]
	v_lshl_add_u64 v[96:97], v[62:63], 0, s[2:3]
	v_lshl_add_u64 v[4:5], v[180:181], 0, v[12:13]
	v_lshl_add_u64 v[8:9], v[180:181], 0, v[14:15]
	v_lshl_add_u64 v[12:13], v[182:183], 0, v[12:13]
	v_lshl_add_u64 v[16:17], v[182:183], 0, v[14:15]
	v_lshl_add_u64 v[20:21], v[180:181], 0, v[62:63]
	v_lshl_add_u64 v[24:25], v[180:181], 0, v[96:97]
	global_load_dwordx4 v[4:7], v[4:5], off
	s_nop 0
	global_load_dwordx4 v[8:11], v[8:9], off
	s_nop 0
	global_load_dwordx4 v[12:15], v[12:13], off
	s_nop 0
	global_load_dwordx4 v[16:19], v[16:17], off
	s_nop 0
	global_load_dwordx4 v[20:23], v[20:21], off
	s_nop 0
	global_load_dwordx4 v[24:27], v[24:25], off
	v_or_b32_e32 v1, s15, v1
	s_movk_i32 s16, 0x140
	v_mul_u32_u24_e32 v0, 0x110, v0
	v_mul_lo_u32 v198, v186, s24
	v_mul_lo_u32 v199, v186, s16
	v_lshlrev_b32_e32 v1, 1, v1
	v_add_u32_e32 v200, 0, v144
	v_xor_b32_e32 v64, 0x80000000, v2
	v_add_u32_e32 v2, 0x2800, v199
	v_add3_u32 v197, 0, v0, v1
	v_add_u32_e32 v144, v200, v198
	v_add_u32_e32 v194, v200, v199
	v_add_u32_e32 v195, v200, v2
	v_mov_b32_e32 v65, v64
	v_mov_b32_e32 v66, v64
	v_mov_b32_e32 v67, v64
	v_mov_b32_e32 v68, v64
	v_mov_b32_e32 v69, v64
	v_mov_b32_e32 v70, v64
	v_mov_b32_e32 v71, v64
	v_mov_b32_e32 v72, v64
	v_mov_b32_e32 v73, v64
	v_mov_b32_e32 v74, v64
	v_mov_b32_e32 v75, v64
	v_mov_b32_e32 v76, v64
	v_mov_b32_e32 v77, v64
	v_mov_b32_e32 v78, v64
	v_mov_b32_e32 v79, v64
	v_and_b32_e32 v193, 63, v32
	v_and_b32_e32 v33, 16, v32
	s_mov_b32 s15, 0x8000
	s_mov_b32 s2, 4
	s_mov_b32 s3, 0
	s_add_i32 s5, s4, 0x8080
	s_add_i32 s4, s4, 0x80c0
	s_waitcnt vmcnt(5)
	ds_write_b128 v144, v[4:7]
	s_waitcnt vmcnt(4)
	ds_write_b128 v144, v[8:11] offset:8704
	s_waitcnt vmcnt(3)
	ds_write_b128 v194, v[12:15] offset:34816
	s_waitcnt vmcnt(2)
	ds_write_b128 v195, v[16:19] offset:34816
	s_waitcnt vmcnt(1)
	ds_write_b128 v144, v[20:23] offset:17408
	s_waitcnt vmcnt(0)
	ds_write_b128 v144, v[24:27] offset:26112
	s_waitcnt lgkmcnt(0)
	s_barrier
	v_readfirstlane_b32 s72, v180
	v_readfirstlane_b32 s73, v181
	v_readfirstlane_b32 s74, v182
	v_readfirstlane_b32 s75, v183
	v_lshl_add_u32 v178, v186, 10, v200
	s_add_i32 s42, s4, 0xffffff40
	s_add_i32 s43, s4, 0xffff7f40
	s_lshl_b32 s43, s43, 3
	s_add_i32 s43, s43, 0xffffff00
	v_bfe_u32 v186, v193, 2, 2
	v_lshrrev_b32_e32 v187, 5, v193
	v_lshl_add_u32 v186, v187, 2, v186
	v_mul_u32_u24_e32 v196, 0x140, v186
	v_bfe_u32 v187, v193, 4, 1
	v_and_b32_e32 v188, 3, v193
	v_lshl_add_u32 v196, v188, 3, v196
	v_lshl_add_u32 v196, v187, 5, v196
	ds_read_b128 v[128:131], v197 offset:0
	ds_read_b128 v[162:165], v197 offset:8704
	ds_read_b128 v[132:135], v197 offset:32
	ds_read_b128 v[166:169], v197 offset:8736
	ds_read_b128 v[136:139], v197 offset:64
	ds_read_b128 v[170:173], v197 offset:8768
	ds_read_b128 v[140:143], v197 offset:96
	ds_read_b128 v[174:177], v197 offset:8800
	v_mov_b32_e32 v0, 0
	v_mov_b32_e32 v1, 0
	v_mov_b32_e32 v2, 0
	v_mov_b32_e32 v3, 0
	v_mov_b32_e32 v4, 0
	v_mov_b32_e32 v5, 0
	v_mov_b32_e32 v6, 0
	v_mov_b32_e32 v7, 0
	v_mov_b32_e32 v8, 0
	v_mov_b32_e32 v9, 0
	v_mov_b32_e32 v10, 0
	v_mov_b32_e32 v11, 0
	v_mov_b32_e32 v12, 0
	v_mov_b32_e32 v13, 0
	v_mov_b32_e32 v14, 0
	v_mov_b32_e32 v15, 0
	v_mov_b32_e32 v16, 0
	v_mov_b32_e32 v17, 0
	v_mov_b32_e32 v18, 0
	v_mov_b32_e32 v19, 0
	v_mov_b32_e32 v20, 0
	v_mov_b32_e32 v21, 0
	v_mov_b32_e32 v22, 0
	v_mov_b32_e32 v23, 0
	v_mov_b32_e32 v24, 0
	v_mov_b32_e32 v25, 0
	v_mov_b32_e32 v26, 0
	v_mov_b32_e32 v27, 0
	v_mov_b32_e32 v28, 0
	v_mov_b32_e32 v29, 0
	v_mov_b32_e32 v30, 0
	v_mov_b32_e32 v31, 0
	v_mov_b32_e32 v32, 0
	v_mov_b32_e32 v33, 0
	v_mov_b32_e32 v34, 0
	v_mov_b32_e32 v35, 0
	v_mov_b32_e32 v36, 0
	v_mov_b32_e32 v37, 0
	v_mov_b32_e32 v38, 0
	v_mov_b32_e32 v39, 0
	v_mov_b32_e32 v40, 0
	v_mov_b32_e32 v41, 0
	v_mov_b32_e32 v42, 0
	v_mov_b32_e32 v43, 0
	v_mov_b32_e32 v44, 0
	v_mov_b32_e32 v45, 0
	v_mov_b32_e32 v46, 0
	v_mov_b32_e32 v47, 0
	v_mov_b32_e32 v48, 0
	v_mov_b32_e32 v49, 0
	v_mov_b32_e32 v50, 0
	v_mov_b32_e32 v51, 0
	v_mov_b32_e32 v52, 0
	v_mov_b32_e32 v53, 0
	v_mov_b32_e32 v54, 0
	v_mov_b32_e32 v55, 0
	v_mov_b32_e32 v56, 0
	v_mov_b32_e32 v57, 0
	v_mov_b32_e32 v58, 0
	v_mov_b32_e32 v59, 0
	v_mov_b32_e32 v60, 0
	v_mov_b32_e32 v61, 0
	v_mov_b32_e32 v62, 0
	v_mov_b32_e32 v63, 0
	v_mov_b32_e32 v201, 0
	s_mov_b32 s2, 0
	s_waitcnt lgkmcnt(6)
	v_mfma_f32_32x32x16_bf16 v[80:95], v[128:131], v[158:161], v[64:79]
	v_mfma_f32_32x32x16_bf16 v[96:111], v[162:165], v[158:161], v[64:79]
	s_waitcnt lgkmcnt(4)
	v_mfma_f32_32x32x16_bf16 v[80:95], v[132:135], v[154:157], v[80:95]
	v_mfma_f32_32x32x16_bf16 v[96:111], v[166:169], v[154:157], v[96:111]
	s_waitcnt lgkmcnt(2)
	v_mfma_f32_32x32x16_bf16 v[80:95], v[136:139], v[150:153], v[80:95]
	v_mfma_f32_32x32x16_bf16 v[96:111], v[170:173], v[150:153], v[96:111]
	s_waitcnt lgkmcnt(0)
	v_mfma_f32_32x32x16_bf16 v[80:95], v[140:143], v[146:149], v[80:95]
	v_mfma_f32_32x32x16_bf16 v[96:111], v[174:177], v[146:149], v[96:111]
	s_cmp_lt_u32 s12, 4
	s_cbranch_scc1 .Latt_lead0
	s_barrier
; #define LAS __attribute__((address_space(3)))
; __device__ __forceinline__ unsigned pk2(float lo, float hi) { f32x2_t v = {lo, hi}; bf16x2_t b = __builtin_convertvector(v, bf16x2_t); return __builtin_bit_cast(unsigned, b); }
; #define AT_LOADK(t) do { const int kr_ = AT_KROW(t); _Pragma("unroll") for (int i_ = 0; i_ < 2; ++i_) kreg[i_] = *(const u32x4*)(Kp + (size_t)(kr_ + prow0 + 32 * i_) * 512 + pch * 8); } while (0)
; #define AT_LOADV(t) do { const int kr_ = AT_KROW(t); _Pragma("unroll") for (int i_ = 0; i_ < 2; ++i_) vreg[i_] = *(const u32x4*)(Vp + (size_t)(kr_ + prow0 + 32 * i_) * 512 + pch * 8); } while (0)
; __device__ __forceinline__ void attn_unit(const Frame& F, int layer, int qrow0, int ntiles, int b, int head, float lam, float m2, float lam_init) {
;     ...
;     for (int t = 0; t < ntiles; ++t) {
;         if (t + 2 < ntiles) AT_LOADK(t + 2);
;         if (t + 1 < ntiles) AT_LOADV(t + 1);
;         if (t + 1 < ntiles) AT_QK(na, nb, (t + 1) & 1);
;         float ls = 0.f;
; #pragma unroll
;         for (int i = 0; i < 16; ++i) { sa[i] = __builtin_amdgcn_exp2f(sa[i]); sb[i] = __builtin_amdgcn_exp2f(sb[i]); ls += sa[i] + sb[i]; }
;         lsum += ls;
;         bf16x8 pk[4];
;         { u32x4 w0, w1, w2, w3;
; #pragma unroll
;           for (int i = 0; i < 4; ++i) { w0[i] = pk2(sa[2 * i], sa[2 * i + 1]); w1[i] = pk2(sa[8 + 2 * i], sa[9 + 2 * i]); w2[i] = pk2(sb[2 * i], sb[2 * i + 1]); w3[i] = pk2(sb[8 + 2 * i], sb[9 + 2 * i]); }
;           pk[0] = __builtin_bit_cast(bf16x8, w0); pk[1] = __builtin_bit_cast(bf16x8, w1); pk[2] = __builtin_bit_cast(bf16x8, w2); pk[3] = __builtin_bit_cast(bf16x8, w3); }
;         LAS const unsigned char* Vt = L + AT_V + (t & 1) * AT_VBYTES;
;         __builtin_amdgcn_sched_barrier(0);
;         bf16x8 vfa[4], vfb[4];
; #pragma unroll
;         for (int j = 0; j < 4; ++j) vfa[j] = frag_tr_acc(Vt, AT_VSTR, 0, 32 * j, lane);
.Latt_lead0:
	s_nop 7
	s_nop 7
.Latt_loop:
	s_add_i32 s5, s2, 2
	s_cmp_ge_u32 s5, 36
	s_cbranch_scc1 .Latt_nokload
	s_cmp_lt_u32 s5, 4
	s_cselect_b32 s15, s42, s43
	s_lshl_b32 s45, s5, 6
	s_add_i32 s15, s15, s45
	s_lshl_b32 s15, s15, 10
	v_add_u32_e32 v186, s15, v178
	v_add_u32_e32 v187, 0x8000, v186
	global_load_dwordx4 v[234:237], v186, s[72:73]
	global_load_dwordx4 v[238:241], v187, s[72:73]
.Latt_nokload:
	s_add_i32 s5, s2, 1
	s_cmp_ge_u32 s5, 36
	s_cbranch_scc1 .Latt_novload
	s_cmp_lt_u32 s5, 4
	s_cselect_b32 s15, s42, s43
	s_lshl_b32 s45, s5, 6
	s_add_i32 s15, s15, s45
	s_lshl_b32 s15, s15, 10
	v_add_u32_e32 v188, s15, v178
	v_add_u32_e32 v189, 0x8000, v188
	global_load_dwordx4 v[242:245], v188, s[74:75]
	global_load_dwordx4 v[248:251], v189, s[74:75]
.Latt_novload:
	v_exp_f32_e32 v80, v80
	v_exp_f32_e32 v96, v96
	v_exp_f32_e32 v81, v81
	v_exp_f32_e32 v97, v97
	v_exp_f32_e32 v82, v82
	v_exp_f32_e32 v98, v98
	v_exp_f32_e32 v83, v83
	v_exp_f32_e32 v99, v99
	v_exp_f32_e32 v84, v84
	v_exp_f32_e32 v100, v100
	v_exp_f32_e32 v85, v85
	v_exp_f32_e32 v101, v101
	v_exp_f32_e32 v86, v86
	v_exp_f32_e32 v102, v102
	v_exp_f32_e32 v87, v87
	v_exp_f32_e32 v103, v103
	v_exp_f32_e32 v88, v88
	v_exp_f32_e32 v104, v104
	v_exp_f32_e32 v89, v89
	v_exp_f32_e32 v105, v105
	v_exp_f32_e32 v90, v90
	v_exp_f32_e32 v106, v106
	v_exp_f32_e32 v91, v91
	v_exp_f32_e32 v107, v107
	v_exp_f32_e32 v92, v92
	v_exp_f32_e32 v108, v108
	v_exp_f32_e32 v93, v93
	v_exp_f32_e32 v109, v109
	v_exp_f32_e32 v94, v94
	v_exp_f32_e32 v110, v110
	v_exp_f32_e32 v95, v95
	v_exp_f32_e32 v111, v111
	v_cvt_pk_bf16_f32 v112, v80, v81
	v_cvt_pk_bf16_f32 v113, v82, v83
	v_cvt_pk_bf16_f32 v114, v84, v85
	v_cvt_pk_bf16_f32 v115, v86, v87
	v_cvt_pk_bf16_f32 v116, v88, v89
	v_cvt_pk_bf16_f32 v117, v90, v91
	v_cvt_pk_bf16_f32 v118, v92, v93
	v_cvt_pk_bf16_f32 v119, v94, v95
	v_cvt_pk_bf16_f32 v120, v96, v97
	v_cvt_pk_bf16_f32 v121, v98, v99
	v_cvt_pk_bf16_f32 v122, v100, v101
	v_cvt_pk_bf16_f32 v123, v102, v103
	v_cvt_pk_bf16_f32 v124, v104, v105
	v_cvt_pk_bf16_f32 v125, v106, v107
	v_cvt_pk_bf16_f32 v126, v108, v109
	v_cvt_pk_bf16_f32 v127, v110, v111
	v_add_f32_e32 v80, v80, v96
	v_add_f32_e32 v81, v81, v97
	v_add_f32_e32 v82, v82, v98
	v_add_f32_e32 v83, v83, v99
	v_add_f32_e32 v84, v84, v100
	v_add_f32_e32 v85, v85, v101
	v_add_f32_e32 v86, v86, v102
	v_add_f32_e32 v87, v87, v103
	v_add_f32_e32 v88, v88, v104
	v_add_f32_e32 v89, v89, v105
	v_add_f32_e32 v90, v90, v106
	v_add_f32_e32 v91, v91, v107
	v_add_f32_e32 v92, v92, v108
	v_add_f32_e32 v93, v93, v109
	v_add_f32_e32 v94, v94, v110
	v_add_f32_e32 v95, v95, v111
	v_add_f32_e32 v80, v80, v88
	v_add_f32_e32 v81, v81, v89
	v_add_f32_e32 v82, v82, v90
	v_add_f32_e32 v83, v83, v91
	v_add_f32_e32 v84, v84, v92
	v_add_f32_e32 v85, v85, v93
	v_add_f32_e32 v86, v86, v94
	v_add_f32_e32 v87, v87, v95
	v_add_f32_e32 v80, v80, v84
	v_add_f32_e32 v81, v81, v85
	v_add_f32_e32 v82, v82, v86
	v_add_f32_e32 v83, v83, v87
	v_add_f32_e32 v80, v80, v82
	v_add_f32_e32 v81, v81, v83
	v_add_f32_e32 v80, v80, v81
	v_add_f32_e32 v201, v201, v80
	s_and_b32 s5, s2, 1
	s_mul_i32 s15, s5, 0x5000
	v_add_u32_e32 v191, s15, v196
	s_mul_i32 s15, s5, 0x4400
	v_add_u32_e32 v179, s15, v144
	s_xor_b32 s5, s5, 1
	s_mul_i32 s15, s5, 0x4400
	v_add_u32_e32 v190, s15, v197
	s_mul_i32 s15, s5, 0x5000
	v_add_u32_e32 v185, s15, v194
	s_barrier
	s_add_i32 s5, s2, 1
	s_cmp_ge_u32 s5, 36
	s_cbranch_scc1 .Latt_noqk
	ds_read_b128 v[128:131], v190 offset:0
	ds_read_b128 v[162:165], v190 offset:8704
	ds_read_b128 v[132:135], v190 offset:32
	ds_read_b128 v[166:169], v190 offset:8736
	ds_read_b128 v[136:139], v190 offset:64
	ds_read_b128 v[170:173], v190 offset:8768
	ds_read_b128 v[140:143], v190 offset:96
	ds_read_b128 v[174:177], v190 offset:8800
	s_waitcnt lgkmcnt(6)
	v_mfma_f32_32x32x16_bf16 v[80:95], v[128:131], v[158:161], v[64:79]
	v_mfma_f32_32x32x16_bf16 v[96:111], v[162:165], v[158:161], v[64:79]
	s_waitcnt lgkmcnt(4)
	v_mfma_f32_32x32x16_bf16 v[80:95], v[132:135], v[154:157], v[80:95]
	v_mfma_f32_32x32x16_bf16 v[96:111], v[166:169], v[154:157], v[96:111]
	ds_read_b64_tr_b16 v[202:203], v191 offset:34816
	ds_read_b64_tr_b16 v[206:207], v191 offset:34880
	ds_read_b64_tr_b16 v[210:211], v191 offset:34944
	ds_read_b64_tr_b16 v[214:215], v191 offset:35008
	ds_read_b64_tr_b16 v[204:205], v191 offset:37376
	ds_read_b64_tr_b16 v[208:209], v191 offset:37440
	ds_read_b64_tr_b16 v[212:213], v191 offset:37504
	ds_read_b64_tr_b16 v[216:217], v191 offset:37568
	s_waitcnt lgkmcnt(10)
	v_mfma_f32_32x32x16_bf16 v[80:95], v[136:139], v[150:153], v[80:95]
	v_mfma_f32_32x32x16_bf16 v[96:111], v[170:173], v[150:153], v[96:111]
	s_waitcnt lgkmcnt(8)
	v_mfma_f32_32x32x16_bf16 v[80:95], v[140:143], v[146:149], v[80:95]
	v_mfma_f32_32x32x16_bf16 v[96:111], v[174:177], v[146:149], v[96:111]
	s_branch .Latt_pv
; #define LAS __attribute__((address_space(3)))
; __device__ __forceinline__ float shx(float v, int m, int lane) { return __int_as_float(__builtin_amdgcn_ds_bpermute((lane ^ m) << 2, __float_as_int(v))); }
; #define MFMA32(a, b, c) __builtin_amdgcn_mfma_f32_32x32x16_bf16((a), (b), (c), 0, 0, 0)
; #define AT_STOREK(st) do { _Pragma("unroll") for (int i_ = 0; i_ < 2; ++i_) *(LAS u32x4*)(L + AT_K + (st) * AT_KBYTES + (prow0 + 32 * i_) * AT_KSTR + pch * 16) = kreg[i_]; } while (0)
; #define AT_STOREV(st) do { _Pragma("unroll") for (int i_ = 0; i_ < 2; ++i_) *(LAS u32x4*)(L + AT_V + (st) * AT_VBYTES + (prow0 + 32 * i_) * AT_VSTR + pch * 16) = vreg[i_]; } while (0)
; __device__ __forceinline__ void attn_unit(const Frame& F, int layer, int qrow0, int ntiles, int b, int head, float lam, float m2, float lam_init) {
;     ...
;         LAS const unsigned char* Vt = L + AT_V + (t & 1) * AT_VBYTES;
;         __builtin_amdgcn_sched_barrier(0);
;         bf16x8 vfa[4], vfb[4];
; #pragma unroll
;         for (int j = 0; j < 4; ++j) vfa[j] = frag_tr_acc(Vt, AT_VSTR, 0, 32 * j, lane);
; #pragma unroll
;         for (int ks = 0; ks < 4; ks += 2) {
; #pragma unroll
;             for (int j = 0; j < 4; ++j) vfb[j] = frag_tr_acc(Vt, AT_VSTR, 16 * (ks + 1), 32 * j, lane);
; #pragma unroll
;             for (int j = 0; j < 4; ++j) o[j] = MFMA32(pk[ks], vfa[j], o[j]);
;             __builtin_amdgcn_sched_barrier(0);
;             if (ks + 2 < 4) {
; #pragma unroll
;                 for (int j = 0; j < 4; ++j) vfa[j] = frag_tr_acc(Vt, AT_VSTR, 16 * (ks + 2), 32 * j, lane);
;             }
; #pragma unroll
;             for (int j = 0; j < 4; ++j) o[j] = MFMA32(pk[ks + 1], vfb[j], o[j]);
;             __builtin_amdgcn_sched_barrier(0);
;         }
;         if (t + 2 < ntiles) AT_STOREK(t & 1);
;         if (t + 1 < ntiles) AT_STOREV((t + 1) & 1);
;         __syncthreads();
;         sa = na; sb = nb;
;     }
;     ...
;     __builtin_amdgcn_s_setprio(0);
;     int lane_e = lane; asm volatile("" : "+v"(lane_e));
;     ...
;     const int r32e = lane_e & 31, hhe = lane_e >> 5;
;     LAS float* lx = (LAS float*)(L + AT_LX + wave * 256);
;     { const float l0 = lsum + shx(lsum, 32, lane_e); if (hh == 0) lx[r32] = (mp ? lam : 1.f) / l0; }
.Latt_noqk:
	ds_read_b64_tr_b16 v[202:203], v191 offset:34816
	ds_read_b64_tr_b16 v[206:207], v191 offset:34880
	ds_read_b64_tr_b16 v[210:211], v191 offset:34944
	ds_read_b64_tr_b16 v[214:215], v191 offset:35008
	ds_read_b64_tr_b16 v[204:205], v191 offset:37376
	ds_read_b64_tr_b16 v[208:209], v191 offset:37440
	ds_read_b64_tr_b16 v[212:213], v191 offset:37504
	ds_read_b64_tr_b16 v[216:217], v191 offset:37568
.Latt_pv:
	s_waitcnt lgkmcnt(3)
	v_mfma_f32_32x32x16_bf16 v[32:47], v[112:115], v[202:205], v[32:47]
	s_waitcnt lgkmcnt(2)
	v_mfma_f32_32x32x16_bf16 v[48:63], v[112:115], v[206:209], v[48:63]
	s_waitcnt lgkmcnt(1)
	v_mfma_f32_32x32x16_bf16 v[0:15], v[112:115], v[210:213], v[0:15]
	ds_read_b64_tr_b16 v[218:219], v191 offset:39936
	ds_read_b64_tr_b16 v[222:223], v191 offset:40000
	ds_read_b64_tr_b16 v[226:227], v191 offset:40064
	ds_read_b64_tr_b16 v[230:231], v191 offset:40128
	ds_read_b64_tr_b16 v[220:221], v191 offset:42496
	ds_read_b64_tr_b16 v[224:225], v191 offset:42560
	ds_read_b64_tr_b16 v[228:229], v191 offset:42624
	ds_read_b64_tr_b16 v[232:233], v191 offset:42688
	s_waitcnt lgkmcnt(8)
	v_mfma_f32_32x32x16_bf16 v[16:31], v[112:115], v[214:217], v[16:31]
	s_waitcnt lgkmcnt(3)
	v_mfma_f32_32x32x16_bf16 v[32:47], v[116:119], v[218:221], v[32:47]
	s_waitcnt lgkmcnt(2)
	v_mfma_f32_32x32x16_bf16 v[48:63], v[116:119], v[222:225], v[48:63]
	s_waitcnt lgkmcnt(1)
	v_mfma_f32_32x32x16_bf16 v[0:15], v[116:119], v[226:229], v[0:15]
	ds_read_b64_tr_b16 v[202:203], v191 offset:45056
	ds_read_b64_tr_b16 v[206:207], v191 offset:45120
	ds_read_b64_tr_b16 v[210:211], v191 offset:45184
	ds_read_b64_tr_b16 v[214:215], v191 offset:45248
	ds_read_b64_tr_b16 v[204:205], v191 offset:47616
	ds_read_b64_tr_b16 v[208:209], v191 offset:47680
	ds_read_b64_tr_b16 v[212:213], v191 offset:47744
	ds_read_b64_tr_b16 v[216:217], v191 offset:47808
	s_waitcnt lgkmcnt(8)
	v_mfma_f32_32x32x16_bf16 v[16:31], v[116:119], v[230:233], v[16:31]
	s_waitcnt lgkmcnt(3)
	v_mfma_f32_32x32x16_bf16 v[32:47], v[120:123], v[202:205], v[32:47]
	s_waitcnt lgkmcnt(2)
	v_mfma_f32_32x32x16_bf16 v[48:63], v[120:123], v[206:209], v[48:63]
	s_waitcnt lgkmcnt(1)
	v_mfma_f32_32x32x16_bf16 v[0:15], v[120:123], v[210:213], v[0:15]
	ds_read_b64_tr_b16 v[218:219], v191 offset:50176
	ds_read_b64_tr_b16 v[222:223], v191 offset:50240
	ds_read_b64_tr_b16 v[226:227], v191 offset:50304
	ds_read_b64_tr_b16 v[230:231], v191 offset:50368
	ds_read_b64_tr_b16 v[220:221], v191 offset:52736
	ds_read_b64_tr_b16 v[224:225], v191 offset:52800
	ds_read_b64_tr_b16 v[228:229], v191 offset:52864
	ds_read_b64_tr_b16 v[232:233], v191 offset:52928
	s_waitcnt lgkmcnt(8)
	v_mfma_f32_32x32x16_bf16 v[16:31], v[120:123], v[214:217], v[16:31]
	s_waitcnt lgkmcnt(3)
	v_mfma_f32_32x32x16_bf16 v[32:47], v[124:127], v[218:221], v[32:47]
	s_waitcnt lgkmcnt(2)
	v_mfma_f32_32x32x16_bf16 v[48:63], v[124:127], v[222:225], v[48:63]
	s_waitcnt lgkmcnt(1)
	v_mfma_f32_32x32x16_bf16 v[0:15], v[124:127], v[226:229], v[0:15]
	s_waitcnt lgkmcnt(0)
	v_mfma_f32_32x32x16_bf16 v[16:31], v[124:127], v[230:233], v[16:31]
	s_waitcnt vmcnt(0)
	s_add_i32 s5, s2, 2
	s_cmp_ge_u32 s5, 36
	s_cbranch_scc1 .Latt_nokst
	ds_write_b128 v179, v[234:237]
	ds_write_b128 v179, v[238:241] offset:8704
.Latt_nokst:
	s_add_i32 s5, s2, 1
	s_cmp_ge_u32 s5, 36
	s_cbranch_scc1 .Latt_novst
	ds_write_b128 v185, v[242:245] offset:34816
	ds_write_b128 v185, v[248:251] offset:45056
.Latt_novst:
	s_waitcnt lgkmcnt(0)
	s_barrier
	s_add_i32 s2, s2, 1
	s_cmp_lt_u32 s2, 36
	s_cbranch_scc1 .Latt_loop
	s_cmp_ge_u32 s12, 4
	s_cbranch_scc1 .Latt_trail1
	s_barrier
.Latt_trail1:
	s_nop 7
	s_nop 7
	v_mov_b32_e32 v64, v201
	s_setprio 0
	s_lshl_b32 s2, s12, 8
	v_lshlrev_b32_e32 v86, 2, v193
	v_xor_b32_e32 v65, 0x80, v86
	ds_bpermute_b32 v65, v65, v64
	s_add_i32 s4, s2, 0
	v_and_b32_e32 v80, 31, v193
	s_add_i32 s4, s4, 0x12800
	v_cmp_gt_u32_e32 vcc, 32, v193
	s_and_saveexec_b64 s[2:3], vcc
	s_cbranch_execz .LBB0_553
	s_cmp_lg_u32 s10, 0
	s_waitcnt lgkmcnt(0)
	v_add_f32_e32 v64, v64, v65
	v_mov_b32_e32 v65, s19
	s_cselect_b64 vcc, -1, 0
	v_cndmask_b32_e32 v65, 1.0, v65, vcc
	v_div_scale_f32 v66, s[12:13], v64, v64, v65
	v_rcp_f32_e32 v67, v66
	s_nop 0
	v_fma_f32 v68, -v66, v67, 1.0
	v_fmac_f32_e32 v67, v68, v67
	v_div_scale_f32 v68, vcc, v65, v64, v65
	v_mul_f32_e32 v69, v68, v67
	v_fma_f32 v70, -v66, v69, v68
	v_fmac_f32_e32 v69, v70, v67
	v_fma_f32 v66, -v66, v69, v68
	v_div_fmas_f32 v66, v66, v67, v69
	v_div_fixup_f32 v64, v66, v64, v65
	v_lshl_add_u32 v65, v80, 2, s4
	ds_write_b32 v65, v64
